# agg2: 16-lane sum of squares via DPP quad_perm/row_ror instead of four ds_bpermute round trips
# baseline (speedup 1.0000x reference)
.LBB3_13:
	s_or_b64 exec, exec, s[2:3]
	v_cvt_f32_u32_e32 v12, v50
	s_waitcnt vmcnt(0)
	v_lshlrev_b32_e32 v13, 16, v2
	v_and_b32_e32 v2, 0xffff0000, v2
	v_lshlrev_b32_e32 v16, 16, v3
	v_max_f32_e32 v12, 1.0, v12
	v_rcp_f32_e32 v12, v12
	v_and_b32_e32 v3, 0xffff0000, v3
	s_load_dwordx2 s[0:1], s[0:1], 0x20
	v_fmac_f32_e32 v2, v12, v11
	v_fmac_f32_e32 v16, v12, v8
	v_lshlrev_b32_e32 v8, 16, v4
	v_fmac_f32_e32 v13, v12, v10
	v_fmac_f32_e32 v8, v12, v0
	v_mul_f32_e32 v0, v2, v2
	v_fmac_f32_e32 v0, v13, v13
	v_fmac_f32_e32 v3, v12, v9
	v_fmac_f32_e32 v0, v16, v16
	v_and_b32_e32 v4, 0xffff0000, v4
	v_fmac_f32_e32 v0, v3, v3
	v_fmac_f32_e32 v4, v12, v1
	v_lshlrev_b32_e32 v9, 16, v5
	v_fmac_f32_e32 v0, v8, v8
	v_fmac_f32_e32 v9, v12, v14
	v_and_b32_e32 v5, 0xffff0000, v5
	v_fmac_f32_e32 v0, v4, v4
	v_fmac_f32_e32 v5, v12, v15
	v_fmac_f32_e32 v0, v9, v9
	v_fmac_f32_e32 v0, v5, v5
	s_nop 1
	v_add_f32_dpp v1, v0, v0 quad_perm:[1,0,3,2] row_mask:0xf bank_mask:0xf
	s_nop 1
	v_add_f32_dpp v0, v1, v1 quad_perm:[2,3,0,1] row_mask:0xf bank_mask:0xf
	s_nop 1
	v_add_f32_dpp v1, v0, v0 row_ror:4 row_mask:0xf bank_mask:0xf
	s_nop 1
	v_add_f32_dpp v0, v1, v1 row_ror:8 row_mask:0xf bank_mask:0xf
	s_waitcnt lgkmcnt(0)
	v_max_f32_e32 v0, 0x179abe15, v0
	v_rsq_f32_e32 v7, v0
	s_nop 0
	v_mul_f32_e32 v4, v4, v7
	v_mul_f32_e32 v0, v13, v7
	v_mul_f32_e32 v1, v2, v7
	v_mul_f32_e32 v2, v16, v7
	v_mul_f32_e32 v3, v3, v7
	v_mul_f32_e32 v4, 0xbfb8aa3b, v4
	v_mul_f32_e32 v9, v9, v7
	v_mul_f32_e32 v0, 0xbfb8aa3b, v0
	v_mul_f32_e32 v1, 0xbfb8aa3b, v1
	v_mul_f32_e32 v2, 0xbfb8aa3b, v2
	v_mul_f32_e32 v3, 0xbfb8aa3b, v3
	v_mul_f32_e32 v8, v8, v7
	v_exp_f32_e32 v4, v4
	v_mul_f32_e32 v9, 0xbfb8aa3b, v9
	v_mul_f32_e32 v5, v5, v7
	v_exp_f32_e32 v0, v0
	v_exp_f32_e32 v1, v1
	v_exp_f32_e32 v2, v2
	v_exp_f32_e32 v3, v3
	v_mul_f32_e32 v8, 0xbfb8aa3b, v8
	v_exp_f32_e32 v10, v9
	v_mul_f32_e32 v5, 0xbfb8aa3b, v5
	v_exp_f32_e32 v8, v8
	v_exp_f32_e32 v5, v5
	v_add_f32_e32 v4, 1.0, v4
	v_add_f32_e32 v0, 1.0, v0
	v_add_f32_e32 v1, 1.0, v1
	v_add_f32_e32 v2, 1.0, v2
	v_add_f32_e32 v3, 1.0, v3
	v_rcp_f32_e32 v9, v4
	v_add_f32_e32 v4, 1.0, v10
	v_rcp_f32_e32 v0, v0
	v_rcp_f32_e32 v1, v1
	v_rcp_f32_e32 v2, v2
	v_rcp_f32_e32 v3, v3
	v_add_f32_e32 v8, 1.0, v8
	v_rcp_f32_e32 v10, v4
	v_add_f32_e32 v4, 1.0, v5
	v_ashrrev_i32_e32 v7, 31, v6
	v_rcp_f32_e32 v8, v8
	v_rcp_f32_e32 v11, v4
	v_lshlrev_b64 v[4:5], 9, v[6:7]
	v_lshl_add_u64 v[4:5], s[0:1], 0, v[4:5]
	v_lshlrev_b32_e32 v6, 4, v48
	v_mov_b32_e32 v7, 0
	v_lshl_add_u64 v[4:5], v[4:5], 0, v[6:7]
	global_store_dwordx4 v[4:5], v[0:3], off nt
	global_store_dwordx4 v[4:5], v[8:11], off offset:256 nt
